# speedup vs baseline: 1.0039x; 1.0011x over previous
.LBB4_11:
	ds_bpermute_b32 v74, v72, v55
	ds_bpermute_b32 v78, v72, v53
	ds_bpermute_b32 v100, v72, v55 offset:4
	ds_bpermute_b32 v79, v72, v53 offset:4
	v_add_u32_e32 v71, -2, v71
	v_cmp_ge_i32_e64 s[0:1], 0, v71
	v_add_u32_e32 v72, 8, v72
	s_waitcnt lgkmcnt(0)
	v_ashrrev_i32_e32 v75, 31, v74
	v_ashrrev_i32_e32 v101, 31, v100
	v_lshlrev_b64 v[74:75], 8, v[74:75]
	v_lshlrev_b64 v[100:101], 8, v[100:101]
	v_lshl_add_u64 v[74:75], v[50:51], 0, v[74:75]
	v_lshl_add_u64 v[100:101], v[50:51], 0, v[100:101]
	global_load_dwordx4 v[74:77], v[74:75], off
	global_load_dwordx4 v[100:103], v[100:101], off
	s_or_b64 s[22:23], s[0:1], s[22:23]
	s_waitcnt vmcnt(1)
	v_fmac_f32_e32 v34, v76, v78
	v_fmac_f32_e32 v35, v77, v78
	v_fmac_f32_e32 v36, v74, v78
	v_fmac_f32_e32 v37, v75, v78
	s_waitcnt vmcnt(0)
	v_fmac_f32_e32 v34, v102, v79
	v_fmac_f32_e32 v35, v103, v79
	v_fmac_f32_e32 v36, v100, v79
	v_fmac_f32_e32 v37, v101, v79
	s_andn2_b64 exec, exec, s[22:23]
	s_cbranch_execnz .LBB4_11
	s_or_b64 exec, exec, s[22:23]
